# v52 + k_agg1g2 self-row load de-serialised: issued at loop top, consumed via fma_mix after the ten neighbour gathers are in flight
# speedup vs baseline: 1.0103x; 1.0103x over previous
.LBB2_4:
	v_lshl_or_b32 v60, s33, 17, v111
	s_lshl_b32 s42, s33, 6
	v_lshl_add_u64 v[80:81], v[60:61], 4, v[62:63]
	v_or_b32_e32 v60, s42, v59
	v_lshl_add_u64 v[10:11], v[60:61], 2, s[24:25]
	global_load_dwordx4 v[2:5], v[10:11], off offset:16
	global_load_dwordx4 v[6:9], v[10:11], off
	v_mov_b32_e32 v88, 0
	v_mov_b32_e32 v89, 0
	v_mov_b32_e32 v86, 0
	v_mov_b32_e32 v87, 0
	v_mov_b32_e32 v84, 0
	v_mov_b32_e32 v85, 0
	v_mov_b32_e32 v82, 0
	v_mov_b32_e32 v83, 0
	s_and_saveexec_b64 s[10:11], s[28:29]
	s_cbranch_execz .LBB2_6
	v_lshl_add_u64 v[96:97], v[80:81], 0, v[64:65]
	s_waitcnt lgkmcnt(6)
	global_load_dwordx4 v[96:99], v[96:97], off
.LBB2_6:
	s_or_b64 exec, exec, s[10:11]
	ds_read2_b32 v[10:11], v51 offset1:4
	s_lshl_b32 s10, s33, 21
	s_waitcnt lgkmcnt(7)
	ds_read2_b32 v[12:13], v51 offset0:8 offset1:12
	s_add_u32 s34, s16, s10
	s_addc_u32 s35, s17, 0
	s_waitcnt lgkmcnt(1)
	v_lshl_add_u32 v10, v10, 7, v110
	v_lshl_add_u32 v11, v11, 7, v110
	global_load_dwordx4 v[42:45], v10, s[34:35]
	global_load_dwordx4 v[38:41], v11, s[34:35]
	ds_read2_b32 v[14:15], v51 offset0:16 offset1:20
	s_waitcnt lgkmcnt(1)
	v_lshl_add_u32 v10, v12, 7, v110
	global_load_dwordx4 v[30:33], v10, s[34:35]
	v_lshl_add_u32 v10, v13, 7, v110
	global_load_dwordx4 v[26:29], v10, s[34:35]
	s_waitcnt lgkmcnt(0)
	v_lshl_add_u32 v10, v14, 7, v110
	global_load_dwordx4 v[10:13], v10, s[34:35]
	v_lshl_add_u32 v14, v15, 7, v110
	global_load_dwordx4 v[14:17], v14, s[34:35]
	ds_read2_b32 v[92:93], v114 offset1:4
	ds_read2_b32 v[18:19], v51 offset0:24 offset1:28
	ds_read2_b32 v[90:91], v114 offset0:8 offset1:12
	ds_read2_b32 v[20:21], v51 offset0:32 offset1:36
	ds_read2_b32 v[94:95], v114 offset0:16 offset1:20
	s_waitcnt lgkmcnt(3)
	v_lshl_add_u32 v18, v18, 7, v110
	v_lshl_add_u32 v19, v19, 7, v110
	s_waitcnt lgkmcnt(1)
	v_lshl_add_u32 v20, v20, 7, v110
	v_lshl_add_u32 v22, v21, 7, v110
	global_load_dwordx4 v[46:49], v18, s[34:35]
	global_load_dwordx4 v[34:37], v19, s[34:35]
	s_nop 0
	global_load_dwordx4 v[18:21], v20, s[34:35]
	s_nop 0
	global_load_dwordx4 v[22:25], v22, s[34:35]
	s_and_saveexec_b64 s[10:11], s[28:29]
	s_waitcnt vmcnt(10)
	v_fma_mix_f32 v82, v72, v99, 0 op_sel_hi:[0,1,0]
	v_fma_mix_f32 v83, v73, v99, 0 op_sel:[0,1,0] op_sel_hi:[0,1,0]
	v_fma_mix_f32 v84, v70, v98, 0 op_sel_hi:[0,1,0]
	v_fma_mix_f32 v85, v71, v98, 0 op_sel:[0,1,0] op_sel_hi:[0,1,0]
	v_fma_mix_f32 v86, v68, v97, 0 op_sel_hi:[0,1,0]
	v_fma_mix_f32 v87, v69, v97, 0 op_sel:[0,1,0] op_sel_hi:[0,1,0]
	v_fma_mix_f32 v88, v56, v96, 0 op_sel_hi:[0,1,0]
	v_fma_mix_f32 v89, v57, v96, 0 op_sel:[0,1,0] op_sel_hi:[0,1,0]
	s_or_b64 exec, exec, s[10:11]
	v_mov_b32_e32 v96, v93
	v_mov_b32_e32 v97, v92
	v_mov_b32_e32 v60, v93
	v_mov_b32_e32 v100, v91
	v_mov_b32_e32 v98, v91
	v_mov_b32_e32 v99, v90
	s_waitcnt vmcnt(9)
	v_cvt_f32_f16_sdwa v103, v45 dst_sel:DWORD dst_unused:UNUSED_PAD src0_sel:WORD_1
	s_waitcnt vmcnt(8)
	v_cvt_f32_f16_sdwa v102, v41 dst_sel:DWORD dst_unused:UNUSED_PAD src0_sel:WORD_1
	v_cvt_f32_f16_e32 v106, v42
	v_cvt_f32_f16_sdwa v107, v42 dst_sel:DWORD dst_unused:UNUSED_PAD src0_sel:WORD_1
	v_cvt_f32_f16_e32 v42, v43
	v_cvt_f32_f16_sdwa v43, v43 dst_sel:DWORD dst_unused:UNUSED_PAD src0_sel:WORD_1
	v_cvt_f32_f16_e32 v116, v38
	v_cvt_f32_f16_sdwa v117, v38 dst_sel:DWORD dst_unused:UNUSED_PAD src0_sel:WORD_1
	v_cvt_f32_f16_e32 v122, v44
	v_cvt_f32_f16_sdwa v123, v44 dst_sel:DWORD dst_unused:UNUSED_PAD src0_sel:WORD_1
	v_cvt_f32_f16_e32 v38, v39
	v_cvt_f32_f16_sdwa v39, v39 dst_sel:DWORD dst_unused:UNUSED_PAD src0_sel:WORD_1
	v_cvt_f32_f16_e32 v53, v45
	s_waitcnt vmcnt(7)
	v_cvt_f32_f16_e32 v118, v30
	v_cvt_f32_f16_sdwa v119, v30 dst_sel:DWORD dst_unused:UNUSED_PAD src0_sel:WORD_1
	v_cvt_f32_f16_e32 v44, v40
	v_cvt_f32_f16_sdwa v45, v40 dst_sel:DWORD dst_unused:UNUSED_PAD src0_sel:WORD_1
	v_cvt_f32_f16_e32 v30, v31
	v_cvt_f32_f16_sdwa v31, v31 dst_sel:DWORD dst_unused:UNUSED_PAD src0_sel:WORD_1
	v_cvt_f32_f16_e32 v101, v41
	s_waitcnt vmcnt(6)
	v_cvt_f32_f16_e32 v120, v26
	v_cvt_f32_f16_sdwa v121, v26 dst_sel:DWORD dst_unused:UNUSED_PAD src0_sel:WORD_1
	v_cvt_f32_f16_e32 v40, v32
	v_cvt_f32_f16_sdwa v41, v32 dst_sel:DWORD dst_unused:UNUSED_PAD src0_sel:WORD_1
	v_cvt_f32_f16_e32 v26, v27
	v_cvt_f32_f16_sdwa v27, v27 dst_sel:DWORD dst_unused:UNUSED_PAD src0_sel:WORD_1
	v_cvt_f32_f16_e32 v124, v33
	v_cvt_f32_f16_sdwa v105, v33 dst_sel:DWORD dst_unused:UNUSED_PAD src0_sel:WORD_1
	v_cvt_f32_f16_sdwa v104, v29 dst_sel:DWORD dst_unused:UNUSED_PAD src0_sel:WORD_1
	v_cvt_f32_f16_e32 v32, v28
	v_cvt_f32_f16_sdwa v33, v28 dst_sel:DWORD dst_unused:UNUSED_PAD src0_sel:WORD_1
	v_cvt_f32_f16_e32 v125, v29
	s_waitcnt vmcnt(5)
	v_cvt_f32_f16_e32 v28, v10
	v_cvt_f32_f16_sdwa v29, v10 dst_sel:DWORD dst_unused:UNUSED_PAD src0_sel:WORD_1
	v_cvt_f32_f16_e32 v10, v11
	v_cvt_f32_f16_sdwa v11, v11 dst_sel:DWORD dst_unused:UNUSED_PAD src0_sel:WORD_1
	v_pk_mul_f32 v[96:97], v[96:97], v[102:103]
	v_cvt_f32_f16_e32 v102, v12
	v_cvt_f32_f16_sdwa v103, v12 dst_sel:DWORD dst_unused:UNUSED_PAD src0_sel:WORD_1
	v_cvt_f32_f16_e32 v12, v13
	v_pk_fma_f32 v[42:43], v[92:93], v[42:43], v[86:87] op_sel_hi:[0,1,1]
	v_pk_fma_f32 v[84:85], v[92:93], v[122:123], v[84:85] op_sel_hi:[0,1,1]
	v_pk_fma_f32 v[38:39], v[60:61], v[38:39], v[42:43] op_sel_hi:[0,1,1]
	v_pk_fma_f32 v[42:43], v[60:61], v[44:45], v[84:85] op_sel_hi:[0,1,1]
	v_pk_fma_f32 v[30:31], v[90:91], v[30:31], v[38:39] op_sel_hi:[0,1,1]
	v_pk_fma_f32 v[38:39], v[90:91], v[40:41], v[42:43] op_sel_hi:[0,1,1]
	v_pk_fma_f32 v[26:27], v[100:101], v[26:27], v[30:31] op_sel_hi:[0,1,1]
	s_waitcnt lgkmcnt(0)
	v_pk_fma_f32 v[26:27], v[94:95], v[10:11], v[26:27] op_sel_hi:[0,1,1]
	v_pk_fma_f32 v[10:11], v[100:101], v[32:33], v[38:39] op_sel_hi:[0,1,1]
	v_mul_f32_e32 v32, v94, v12
	v_cvt_f32_f16_sdwa v13, v13 dst_sel:DWORD dst_unused:UNUSED_PAD src0_sel:WORD_1
	s_waitcnt vmcnt(4)
	v_cvt_f32_f16_sdwa v12, v17 dst_sel:DWORD dst_unused:UNUSED_PAD src0_sel:WORD_1
	v_mul_f32_e32 v86, v92, v53
	v_pk_fma_f32 v[30:31], v[94:95], v[102:103], v[10:11] op_sel_hi:[0,1,1]
	v_cvt_f32_f16_e32 v42, v16
	v_cvt_f32_f16_e32 v10, v17
	v_cvt_f32_f16_sdwa v43, v16 dst_sel:DWORD dst_unused:UNUSED_PAD src0_sel:WORD_1
	v_mov_b32_e32 v16, v95
	v_mov_b32_e32 v17, v94
	v_mov_b32_e32 v87, v97
	v_pk_mul_f32 v[98:99], v[98:99], v[104:105]
	v_pk_fma_f32 v[88:89], v[92:93], v[106:107], v[88:89] op_sel_hi:[0,1,1]
	v_mul_f32_e32 v92, v93, v101
	v_pk_mul_f32 v[12:13], v[16:17], v[12:13]
	v_pk_add_f32 v[16:17], v[82:83], v[86:87]
	v_mov_b32_e32 v93, v96
	v_mul_f32_e32 v104, v90, v124
	v_pk_add_f32 v[16:17], v[92:93], v[16:17]
	v_mov_b32_e32 v105, v99
	v_mul_f32_e32 v106, v91, v125
	v_pk_fma_f32 v[88:89], v[60:61], v[116:117], v[88:89] op_sel_hi:[0,1,1]
	v_cvt_f32_f16_e32 v38, v14
	v_cvt_f32_f16_sdwa v39, v14 dst_sel:DWORD dst_unused:UNUSED_PAD src0_sel:WORD_1
	v_pk_add_f32 v[16:17], v[104:105], v[16:17]
	v_mov_b32_e32 v107, v98
	v_pk_fma_f32 v[44:45], v[90:91], v[118:119], v[88:89] op_sel_hi:[0,1,1]
	v_pk_add_f32 v[16:17], v[106:107], v[16:17]
	v_mov_b32_e32 v33, v13
	v_pk_fma_f32 v[40:41], v[100:101], v[120:121], v[44:45] op_sel_hi:[0,1,1]
	v_pk_add_f32 v[16:17], v[32:33], v[16:17]
	ds_read2_b32 v[32:33], v114 offset0:24 offset1:28
	v_pk_fma_f32 v[28:29], v[94:95], v[28:29], v[40:41] op_sel_hi:[0,1,1]
	v_mov_b32_e32 v14, v95
	s_waitcnt vmcnt(3)
	v_cvt_f32_f16_e32 v44, v46
	v_cvt_f32_f16_sdwa v45, v46 dst_sel:DWORD dst_unused:UNUSED_PAD src0_sel:WORD_1
	ds_read2_b32 v[88:89], v114 offset0:32 offset1:36
	v_pk_fma_f32 v[28:29], v[14:15], v[38:39], v[28:29] op_sel_hi:[0,1,1]
	s_waitcnt vmcnt(2)
	v_cvt_f32_f16_e32 v38, v34
	v_cvt_f32_f16_sdwa v39, v34 dst_sel:DWORD dst_unused:UNUSED_PAD src0_sel:WORD_1
	s_waitcnt vmcnt(1)
	v_cvt_f32_f16_e32 v92, v18
	v_cvt_f32_f16_sdwa v93, v18 dst_sel:DWORD dst_unused:UNUSED_PAD src0_sel:WORD_1
	v_mul_f32_e32 v10, v95, v10
	s_waitcnt vmcnt(0)
	v_cvt_f32_f16_e32 v94, v22
	v_cvt_f32_f16_sdwa v95, v22 dst_sel:DWORD dst_unused:UNUSED_PAD src0_sel:WORD_1
	s_waitcnt lgkmcnt(1)
	v_pk_fma_f32 v[28:29], v[32:33], v[44:45], v[28:29] op_sel_hi:[0,1,1]
	v_mov_b32_e32 v44, v33
	v_cvt_f32_f16_e32 v40, v15
	v_cvt_f32_f16_sdwa v41, v15 dst_sel:DWORD dst_unused:UNUSED_PAD src0_sel:WORD_1
	v_pk_fma_f32 v[28:29], v[44:45], v[38:39], v[28:29] op_sel_hi:[0,1,1]
	v_cvt_f32_f16_e32 v46, v47
	v_cvt_f32_f16_sdwa v47, v47 dst_sel:DWORD dst_unused:UNUSED_PAD src0_sel:WORD_1
	s_waitcnt lgkmcnt(0)
	v_pk_fma_f32 v[28:29], v[88:89], v[92:93], v[28:29] op_sel_hi:[0,1,1]
	v_mov_b32_e32 v18, v89
	v_pk_fma_f32 v[38:39], v[18:19], v[94:95], v[28:29] op_sel_hi:[0,1,1]
	v_cvt_f32_f16_e32 v28, v35
	v_cvt_f32_f16_sdwa v29, v35 dst_sel:DWORD dst_unused:UNUSED_PAD src0_sel:WORD_1
	v_cvt_f32_f16_e32 v34, v19
	v_cvt_f32_f16_sdwa v35, v19 dst_sel:DWORD dst_unused:UNUSED_PAD src0_sel:WORD_1
	v_cvt_f32_f16_e32 v11, v49
	v_pk_fma_f32 v[26:27], v[14:15], v[40:41], v[26:27] op_sel_hi:[0,1,1]
	v_cvt_f32_f16_e32 v22, v23
	v_cvt_f32_f16_sdwa v23, v23 dst_sel:DWORD dst_unused:UNUSED_PAD src0_sel:WORD_1
	v_pk_fma_f32 v[26:27], v[32:33], v[46:47], v[26:27] op_sel_hi:[0,1,1]
	v_pk_fma_f32 v[26:27], v[44:45], v[28:29], v[26:27] op_sel_hi:[0,1,1]
	v_cvt_f32_f16_e32 v82, v48
	v_cvt_f32_f16_sdwa v83, v48 dst_sel:DWORD dst_unused:UNUSED_PAD src0_sel:WORD_1
	v_pk_fma_f32 v[26:27], v[88:89], v[34:35], v[26:27] op_sel_hi:[0,1,1]
	v_mul_f32_e32 v48, v32, v11
	v_cvt_f32_f16_sdwa v87, v49 dst_sel:DWORD dst_unused:UNUSED_PAD src0_sel:WORD_1
	v_cvt_f32_f16_sdwa v86, v37 dst_sel:DWORD dst_unused:UNUSED_PAD src0_sel:WORD_1
	v_cvt_f32_f16_e32 v11, v21
	v_pk_fma_f32 v[34:35], v[18:19], v[22:23], v[26:27] op_sel_hi:[0,1,1]
	v_cvt_f32_f16_e32 v22, v36
	v_cvt_f32_f16_sdwa v23, v36 dst_sel:DWORD dst_unused:UNUSED_PAD src0_sel:WORD_1
	v_cvt_f32_f16_e32 v26, v20
	v_cvt_f32_f16_sdwa v27, v20 dst_sel:DWORD dst_unused:UNUSED_PAD src0_sel:WORD_1
	v_pk_fma_f32 v[14:15], v[14:15], v[42:43], v[30:31] op_sel_hi:[0,1,1]
	v_cvt_f32_f16_e32 v28, v24
	v_cvt_f32_f16_sdwa v29, v24 dst_sel:DWORD dst_unused:UNUSED_PAD src0_sel:WORD_1
	v_mov_b32_e32 v90, v33
	v_mov_b32_e32 v91, v32
	v_pk_fma_f32 v[14:15], v[32:33], v[82:83], v[14:15] op_sel_hi:[0,1,1]
	v_pk_mul_f32 v[86:87], v[90:91], v[86:87]
	v_mul_f32_e32 v90, v88, v11
	v_pk_fma_f32 v[14:15], v[44:45], v[22:23], v[14:15] op_sel_hi:[0,1,1]
	v_cvt_f32_f16_e32 v11, v25
	v_pk_fma_f32 v[14:15], v[88:89], v[26:27], v[14:15] op_sel_hi:[0,1,1]
	v_cvt_f32_f16_e32 v13, v37
	v_pk_fma_f32 v[36:37], v[18:19], v[28:29], v[14:15] op_sel_hi:[0,1,1]
	v_cvt_f32_f16_sdwa v15, v21 dst_sel:DWORD dst_unused:UNUSED_PAD src0_sel:WORD_1
	v_cvt_f32_f16_sdwa v14, v25 dst_sel:DWORD dst_unused:UNUSED_PAD src0_sel:WORD_1
	v_mul_f32_e32 v18, v89, v11
	v_mov_b32_e32 v11, v12
	v_mov_b32_e32 v20, v89
	v_mov_b32_e32 v21, v88
	v_pk_add_f32 v[10:11], v[10:11], v[16:17]
	v_mov_b32_e32 v49, v87
	v_mul_f32_e32 v84, v33, v13
	v_pk_mul_f32 v[14:15], v[20:21], v[14:15]
	v_pk_add_f32 v[10:11], v[48:49], v[10:11]
	v_mov_b32_e32 v85, v86
	v_pk_add_f32 v[10:11], v[84:85], v[10:11]
	v_mov_b32_e32 v91, v15
	v_pk_add_f32 v[10:11], v[90:91], v[10:11]
	v_mov_b32_e32 v19, v14
	v_pk_add_f32 v[40:41], v[18:19], v[10:11]
	s_and_saveexec_b64 s[10:11], s[2:3]
	s_cbranch_execz .LBB2_8
	ds_read2_b32 v[10:11], v51 offset0:40 offset1:44
	ds_read2_b32 v[12:13], v51 offset0:48 offset1:52
	ds_read2_b32 v[14:15], v51 offset0:56 offset1:60
	s_waitcnt lgkmcnt(2)
	v_lshl_add_u32 v10, v10, 7, v110
	v_lshl_add_u32 v11, v11, 7, v110
	global_load_dwordx4 v[30:33], v10, s[34:35]
	global_load_dwordx4 v[26:29], v11, s[34:35]
	s_waitcnt lgkmcnt(1)
	v_lshl_add_u32 v10, v12, 7, v110
	v_lshl_add_u32 v11, v13, 7, v110
	global_load_dwordx4 v[22:25], v10, s[34:35]
	global_load_dwordx4 v[18:21], v11, s[34:35]
	s_waitcnt lgkmcnt(0)
	v_lshl_add_u32 v10, v14, 7, v110
	global_load_dwordx4 v[10:13], v10, s[34:35]
	v_lshl_add_u32 v14, v15, 7, v110
	global_load_dwordx4 v[14:17], v14, s[34:35]
	ds_read2_b32 v[44:45], v114 offset0:40 offset1:44
	ds_read2_b32 v[42:43], v114 offset0:48 offset1:52
	ds_read2_b32 v[46:47], v114 offset0:56 offset1:60
	s_waitcnt lgkmcnt(2)
	v_mov_b32_e32 v84, v45
	v_mov_b32_e32 v85, v44
	v_mov_b32_e32 v60, v45
	s_waitcnt lgkmcnt(1)
	v_mov_b32_e32 v82, v43
	v_mov_b32_e32 v83, v42
	v_mov_b32_e32 v86, v43
	s_waitcnt lgkmcnt(0)
	v_mov_b32_e32 v48, v47
	s_waitcnt vmcnt(5)
	v_cvt_f32_f16_e32 v92, v30
	v_cvt_f32_f16_sdwa v93, v30 dst_sel:DWORD dst_unused:UNUSED_PAD src0_sel:WORD_1
	v_cvt_f32_f16_e32 v30, v31
	v_cvt_f32_f16_sdwa v31, v31 dst_sel:DWORD dst_unused:UNUSED_PAD src0_sel:WORD_1
	v_cvt_f32_f16_e32 v104, v32
	v_cvt_f32_f16_sdwa v105, v32 dst_sel:DWORD dst_unused:UNUSED_PAD src0_sel:WORD_1
	v_cvt_f32_f16_e32 v49, v33
	v_cvt_f32_f16_sdwa v89, v33 dst_sel:DWORD dst_unused:UNUSED_PAD src0_sel:WORD_1
	s_waitcnt vmcnt(4)
	v_cvt_f32_f16_sdwa v88, v29 dst_sel:DWORD dst_unused:UNUSED_PAD src0_sel:WORD_1
	v_cvt_f32_f16_e32 v94, v26
	v_cvt_f32_f16_sdwa v95, v26 dst_sel:DWORD dst_unused:UNUSED_PAD src0_sel:WORD_1
	v_cvt_f32_f16_e32 v26, v27
	v_cvt_f32_f16_sdwa v27, v27 dst_sel:DWORD dst_unused:UNUSED_PAD src0_sel:WORD_1
	v_cvt_f32_f16_e32 v32, v28
	v_cvt_f32_f16_sdwa v33, v28 dst_sel:DWORD dst_unused:UNUSED_PAD src0_sel:WORD_1
	v_cvt_f32_f16_e32 v53, v29
	s_waitcnt vmcnt(3)
	v_cvt_f32_f16_e32 v96, v22
	v_cvt_f32_f16_sdwa v97, v22 dst_sel:DWORD dst_unused:UNUSED_PAD src0_sel:WORD_1
	v_cvt_f32_f16_e32 v22, v23
	v_cvt_f32_f16_sdwa v23, v23 dst_sel:DWORD dst_unused:UNUSED_PAD src0_sel:WORD_1
	v_cvt_f32_f16_e32 v28, v24
	v_cvt_f32_f16_sdwa v29, v24 dst_sel:DWORD dst_unused:UNUSED_PAD src0_sel:WORD_1
	v_cvt_f32_f16_e32 v87, v25
	s_waitcnt vmcnt(2)
	v_cvt_f32_f16_e32 v117, v21
	v_cvt_f32_f16_sdwa v91, v25 dst_sel:DWORD dst_unused:UNUSED_PAD src0_sel:WORD_1
	v_cvt_f32_f16_sdwa v90, v21 dst_sel:DWORD dst_unused:UNUSED_PAD src0_sel:WORD_1
	v_cvt_f32_f16_e32 v98, v18
	v_cvt_f32_f16_sdwa v99, v18 dst_sel:DWORD dst_unused:UNUSED_PAD src0_sel:WORD_1
	v_cvt_f32_f16_e32 v18, v19
	v_cvt_f32_f16_sdwa v19, v19 dst_sel:DWORD dst_unused:UNUSED_PAD src0_sel:WORD_1
	v_cvt_f32_f16_e32 v24, v20
	v_cvt_f32_f16_sdwa v25, v20 dst_sel:DWORD dst_unused:UNUSED_PAD src0_sel:WORD_1
	s_waitcnt vmcnt(1)
	v_cvt_f32_f16_e32 v100, v10
	v_cvt_f32_f16_sdwa v101, v10 dst_sel:DWORD dst_unused:UNUSED_PAD src0_sel:WORD_1
	v_cvt_f32_f16_e32 v10, v11
	v_cvt_f32_f16_sdwa v11, v11 dst_sel:DWORD dst_unused:UNUSED_PAD src0_sel:WORD_1
	v_cvt_f32_f16_e32 v20, v12
	v_cvt_f32_f16_sdwa v21, v12 dst_sel:DWORD dst_unused:UNUSED_PAD src0_sel:WORD_1
	v_pk_fma_f32 v[30:31], v[44:45], v[30:31], v[34:35] op_sel_hi:[0,1,1]
	v_pk_fma_f32 v[34:35], v[44:45], v[104:105], v[36:37] op_sel_hi:[0,1,1]
	v_cvt_f32_f16_e32 v119, v13
	v_cvt_f32_f16_sdwa v13, v13 dst_sel:DWORD dst_unused:UNUSED_PAD src0_sel:WORD_1
	s_waitcnt vmcnt(0)
	v_cvt_f32_f16_sdwa v12, v17 dst_sel:DWORD dst_unused:UNUSED_PAD src0_sel:WORD_1
	v_pk_mul_f32 v[84:85], v[84:85], v[88:89]
	v_pk_fma_f32 v[26:27], v[60:61], v[26:27], v[30:31] op_sel_hi:[0,1,1]
	v_pk_fma_f32 v[30:31], v[60:61], v[32:33], v[34:35] op_sel_hi:[0,1,1]
	v_cvt_f32_f16_e32 v106, v16
	v_cvt_f32_f16_sdwa v107, v16 dst_sel:DWORD dst_unused:UNUSED_PAD src0_sel:WORD_1
	v_cvt_f32_f16_e32 v120, v17
	v_mul_f32_e32 v16, v44, v49
	v_pk_fma_f32 v[22:23], v[42:43], v[22:23], v[26:27] op_sel_hi:[0,1,1]
	v_pk_fma_f32 v[26:27], v[42:43], v[28:29], v[30:31] op_sel_hi:[0,1,1]
	v_mov_b32_e32 v17, v85
	v_mul_f32_e32 v116, v45, v53
	v_mul_f32_e32 v118, v43, v117
	v_pk_mul_f32 v[82:83], v[82:83], v[90:91]
	v_pk_fma_f32 v[38:39], v[44:45], v[92:93], v[38:39] op_sel_hi:[0,1,1]
	v_pk_fma_f32 v[18:19], v[86:87], v[18:19], v[22:23] op_sel_hi:[0,1,1]
	v_pk_fma_f32 v[22:23], v[86:87], v[24:25], v[26:27] op_sel_hi:[0,1,1]
	v_pk_add_f32 v[16:17], v[40:41], v[16:17]
	v_mov_b32_e32 v117, v84
	v_cvt_f32_f16_e32 v102, v14
	v_cvt_f32_f16_sdwa v103, v14 dst_sel:DWORD dst_unused:UNUSED_PAD src0_sel:WORD_1
	v_cvt_f32_f16_e32 v14, v15
	v_cvt_f32_f16_sdwa v15, v15 dst_sel:DWORD dst_unused:UNUSED_PAD src0_sel:WORD_1
	v_mul_f32_e32 v88, v42, v87
	v_pk_fma_f32 v[36:37], v[60:61], v[94:95], v[38:39] op_sel_hi:[0,1,1]
	v_pk_fma_f32 v[10:11], v[46:47], v[10:11], v[18:19] op_sel_hi:[0,1,1]
	v_pk_fma_f32 v[18:19], v[46:47], v[20:21], v[22:23] op_sel_hi:[0,1,1]
	v_mov_b32_e32 v22, v47
	v_mov_b32_e32 v23, v46
	v_pk_add_f32 v[16:17], v[116:117], v[16:17]
	v_mov_b32_e32 v89, v83
	v_mul_f32_e32 v90, v46, v119
	v_pk_fma_f32 v[32:33], v[42:43], v[96:97], v[36:37] op_sel_hi:[0,1,1]
	v_pk_mul_f32 v[12:13], v[22:23], v[12:13]
	v_pk_add_f32 v[16:17], v[88:89], v[16:17]
	v_mov_b32_e32 v119, v82
	v_pk_fma_f32 v[28:29], v[86:87], v[98:99], v[32:33] op_sel_hi:[0,1,1]
	v_pk_add_f32 v[16:17], v[118:119], v[16:17]
	v_mov_b32_e32 v91, v13
	v_pk_fma_f32 v[24:25], v[46:47], v[100:101], v[28:29] op_sel_hi:[0,1,1]
	v_mul_f32_e32 v20, v47, v120
	v_pk_add_f32 v[16:17], v[90:91], v[16:17]
	v_mov_b32_e32 v21, v12
	v_pk_fma_f32 v[38:39], v[48:49], v[102:103], v[24:25] op_sel_hi:[0,1,1]
	v_pk_fma_f32 v[34:35], v[48:49], v[14:15], v[10:11] op_sel_hi:[0,1,1]
	v_pk_fma_f32 v[36:37], v[48:49], v[106:107], v[18:19] op_sel_hi:[0,1,1]
	v_pk_add_f32 v[40:41], v[20:21], v[16:17]
